# stack23 = stack22 + small QKV column pass: last four k-steps peeled without the three weight requests beyond K (the pass epilogue waited for them)
# speedup vs baseline: 1.0101x; 1.0032x over previous
; #define LOADP(i_, ks_) do { pa[i_] = *(const bf16x8*)(wb + (size_t)((ks_) * 144) * 1024 + voff); pb[i_] = *(const bf16x8*)(wb + (size_t)((ks_) * 144 + 2) * 1024 + voff); } while (0)
; #define STEP(i_, ks_) do { _Pragma("unroll") for (int mi = 0; mi < 4; ++mi) { const bf16x8 f = AFRAG(mi, ks_); \
;         acc[0][mi] = __builtin_amdgcn_mfma_f32_16x16x32_bf16(pa[i_], f, acc[0][mi], 0, 0, 0); acc[1][mi] = __builtin_amdgcn_mfma_f32_16x16x32_bf16(pb[i_], f, acc[1][mi], 0, 0, 0); } } while (0)
; DEVINL void phase2(const Params& P, unsigned char* smem, XPre& X, const bool have_pre) {
;     ...
;             LOADP(0, 0); LOADP(1, 1); LOADP(2, 2);
; #pragma unroll 1
;             for (int ks = 0; ks < 32; ks += 4) {
;                 LOADP(3, ks + 3);                            __builtin_amdgcn_sched_barrier(0);
;                 STEP(0, ks);     __builtin_amdgcn_sched_barrier(0); LOADP(0, ks + 4 < 32 ? ks + 4 : 31); __builtin_amdgcn_sched_barrier(0);
;                 STEP(1, ks + 1); __builtin_amdgcn_sched_barrier(0); LOADP(1, ks + 5 < 32 ? ks + 5 : 31); __builtin_amdgcn_sched_barrier(0);
;                 STEP(2, ks + 2); __builtin_amdgcn_sched_barrier(0); LOADP(2, ks + 6 < 32 ? ks + 6 : 31); __builtin_amdgcn_sched_barrier(0);
;                 STEP(3, ks + 3); __builtin_amdgcn_sched_barrier(0);
;             }
.LBB0_193:
	v_lshl_add_u64 v[60:61], v[196:197], 0, s[0:1]
	s_mov_b32 s7, 0x46c000
	v_add_co_u32_e32 v64, vcc, s7, v60
	s_nop 1
	v_addc_co_u32_e32 v65, vcc, 0, v61, vcc
	global_load_dwordx4 v[60:63], v[64:65], off
	s_nop 0
	global_load_dwordx4 v[64:67], v[64:65], off offset:2048
	v_add_u32_e32 v104, -4, v58
	v_xor_b32_e32 v104, v104, v181
	v_lshl_add_u32 v104, v104, 4, v212
	v_add_u32_e32 v105, 0x10000, v104
	ds_read_b128 v[86:89], v104
	ds_read_b128 v[90:93], v104 offset:32768
	ds_read_b128 v[94:97], v105
	ds_read_b128 v[98:101], v105 offset:32768
	s_waitcnt vmcnt(7) lgkmcnt(7)
	v_mfma_f32_16x16x32_bf16 v[54:57], v[38:41], v[68:71], v[54:57]
	s_waitcnt vmcnt(6)
	v_mfma_f32_16x16x32_bf16 v[50:53], v[42:45], v[68:71], v[50:53]
	s_waitcnt lgkmcnt(6)
	v_mfma_f32_16x16x32_bf16 v[46:49], v[38:41], v[72:75], v[46:49]
	v_mfma_f32_16x16x32_bf16 v[30:33], v[42:45], v[72:75], v[30:33]
	s_waitcnt lgkmcnt(5)
	v_mfma_f32_16x16x32_bf16 v[14:17], v[38:41], v[76:79], v[14:17]
	v_mfma_f32_16x16x32_bf16 v[10:13], v[42:45], v[76:79], v[10:13]
	s_waitcnt lgkmcnt(4)
	v_mfma_f32_16x16x32_bf16 v[6:9], v[38:41], v[80:83], v[6:9]
	v_mfma_f32_16x16x32_bf16 v[2:5], v[42:45], v[80:83], v[2:5]
	s_add_i32 s7, s6, 4
	s_add_u32 s0, s0, 0x90000
	s_addc_u32 s1, s1, 0
	s_cmp_lt_u32 s6, 28
	s_cselect_b32 s18, s0, 0x45c000
	v_lshl_add_u64 v[42:43], v[184:185], 0, s[18:19]
	global_load_dwordx4 v[38:41], v[42:43], off
	s_nop 0
	global_load_dwordx4 v[42:45], v[42:43], off offset:2048
	s_min_u32 s9, s6, 26
	s_mul_i32 s9, s9, 0x24000
	s_add_u32 s10, s58, s9
	s_addc_u32 s11, s59, 0
	s_min_u32 s9, s6, 25
	s_mul_i32 s9, s9, 0x24000
	s_add_u32 s12, s58, s9
	s_addc_u32 s13, s59, 0
	s_cmp_gt_u32 s6, 23
	v_xor_b32_e32 v104, v58, v181
	v_lshl_add_u32 v104, v104, 4, v212
	v_add_u32_e32 v105, 0x10000, v104
	ds_read_b128 v[68:71], v104
	ds_read_b128 v[72:75], v104 offset:32768
	ds_read_b128 v[76:79], v105
	ds_read_b128 v[80:83], v105 offset:32768
	s_waitcnt vmcnt(7) lgkmcnt(7)
	v_mfma_f32_16x16x32_bf16 v[54:57], v[18:21], v[86:89], v[54:57]
	s_waitcnt vmcnt(6)
	v_mfma_f32_16x16x32_bf16 v[50:53], v[22:25], v[86:89], v[50:53]
	s_waitcnt lgkmcnt(6)
	v_mfma_f32_16x16x32_bf16 v[46:49], v[18:21], v[90:93], v[46:49]
	v_mfma_f32_16x16x32_bf16 v[30:33], v[22:25], v[90:93], v[30:33]
	s_waitcnt lgkmcnt(5)
	v_mfma_f32_16x16x32_bf16 v[14:17], v[18:21], v[94:97], v[14:17]
	v_mfma_f32_16x16x32_bf16 v[10:13], v[22:25], v[94:97], v[10:13]
	s_waitcnt lgkmcnt(4)
	v_mfma_f32_16x16x32_bf16 v[6:9], v[18:21], v[98:101], v[6:9]
	v_mfma_f32_16x16x32_bf16 v[2:5], v[22:25], v[98:101], v[2:5]
	v_lshl_add_u64 v[18:19], s[10:11], 0, v[182:183]
	s_mov_b32 s6, 0xb4000
	v_add_co_u32_e32 v22, vcc, s6, v18
	s_nop 1
	v_addc_co_u32_e32 v23, vcc, 0, v19, vcc
	global_load_dwordx4 v[18:21], v[22:23], off
	s_nop 0
	global_load_dwordx4 v[22:25], v[22:23], off offset:2048
	v_add_u32_e32 v104, 4, v58
	v_xor_b32_e32 v104, v104, v181
	v_lshl_add_u32 v104, v104, 4, v212
	v_add_u32_e32 v105, 0x10000, v104
	ds_read_b128 v[86:89], v104
	ds_read_b128 v[90:93], v104 offset:32768
	ds_read_b128 v[94:97], v105
	ds_read_b128 v[98:101], v105 offset:32768
	s_waitcnt vmcnt(7) lgkmcnt(7)
	v_mfma_f32_16x16x32_bf16 v[54:57], v[26:29], v[68:71], v[54:57]
	s_waitcnt vmcnt(6)
	v_mfma_f32_16x16x32_bf16 v[50:53], v[34:37], v[68:71], v[50:53]
	s_waitcnt lgkmcnt(6)
	v_mfma_f32_16x16x32_bf16 v[46:49], v[26:29], v[72:75], v[46:49]
	v_mfma_f32_16x16x32_bf16 v[30:33], v[34:37], v[72:75], v[30:33]
	s_waitcnt lgkmcnt(5)
	v_mfma_f32_16x16x32_bf16 v[14:17], v[26:29], v[76:79], v[14:17]
	v_mfma_f32_16x16x32_bf16 v[10:13], v[34:37], v[76:79], v[10:13]
	s_waitcnt lgkmcnt(4)
	v_mfma_f32_16x16x32_bf16 v[6:9], v[26:29], v[80:83], v[6:9]
	v_mfma_f32_16x16x32_bf16 v[2:5], v[34:37], v[80:83], v[2:5]
	v_lshl_add_u64 v[26:27], s[12:13], 0, v[182:183]
	s_mov_b32 s6, 0xd8000
	v_add_co_u32_e32 v34, vcc, s6, v26
	s_nop 1
	v_addc_co_u32_e32 v35, vcc, 0, v27, vcc
	global_load_dwordx4 v[26:29], v[34:35], off
	s_nop 0
	global_load_dwordx4 v[34:37], v[34:35], off offset:2048
	v_add_u32_e32 v58, 16, v58
	v_add_u32_e32 v104, -8, v58
	v_xor_b32_e32 v104, v104, v181
	v_lshl_add_u32 v104, v104, 4, v212
	v_add_u32_e32 v105, 0x10000, v104
	ds_read_b128 v[68:71], v104
	ds_read_b128 v[72:75], v104 offset:32768
	ds_read_b128 v[76:79], v105
	ds_read_b128 v[80:83], v105 offset:32768
	s_waitcnt vmcnt(7) lgkmcnt(7)
	v_mfma_f32_16x16x32_bf16 v[54:57], v[60:63], v[86:89], v[54:57]
	s_waitcnt vmcnt(6)
	v_mfma_f32_16x16x32_bf16 v[50:53], v[64:67], v[86:89], v[50:53]
	s_waitcnt lgkmcnt(6)
	v_mfma_f32_16x16x32_bf16 v[46:49], v[60:63], v[90:93], v[46:49]
	v_mfma_f32_16x16x32_bf16 v[30:33], v[64:67], v[90:93], v[30:33]
	s_waitcnt lgkmcnt(5)
	v_mfma_f32_16x16x32_bf16 v[14:17], v[60:63], v[94:97], v[14:17]
	v_mfma_f32_16x16x32_bf16 v[10:13], v[64:67], v[94:97], v[10:13]
	s_waitcnt lgkmcnt(4)
	v_mfma_f32_16x16x32_bf16 v[6:9], v[60:63], v[98:101], v[6:9]
	v_mfma_f32_16x16x32_bf16 v[2:5], v[64:67], v[98:101], v[2:5]
	s_mov_b32 s6, s7
	s_cbranch_scc0 .LBB0_193
; #define LOADP(i_, ks_) do { pa[i_] = *(const bf16x8*)(wb + (size_t)((ks_) * 144) * 1024 + voff); pb[i_] = *(const bf16x8*)(wb + (size_t)((ks_) * 144 + 2) * 1024 + voff); } while (0)
; #define STEP(i_, ks_) do { _Pragma("unroll") for (int mi = 0; mi < 4; ++mi) { const bf16x8 f = AFRAG(mi, ks_); \
;         acc[0][mi] = __builtin_amdgcn_mfma_f32_16x16x32_bf16(pa[i_], f, acc[0][mi], 0, 0, 0); acc[1][mi] = __builtin_amdgcn_mfma_f32_16x16x32_bf16(pb[i_], f, acc[1][mi], 0, 0, 0); } } while (0)
; DEVINL void qkv_store_head(const Params& P, const f32x4 (&v0)[4], int slot, int m, int g, const float* rc, const float* rs, int nfr, int fr0) {
;     ...
;     if (region == 3 || region == 4) {
; #pragma unroll
;         for (int ni = 0; ni < 2; ++ni) if (ni < hp) {
;             const int fr = fr0 + ni * fstep;
;             const f32x4 cs = *(const f32x4*)(rc + sq * 32 + 16 * fr + 4 * g), sn = *(const f32x4*)(rs + sq * 32 + 16 * fr + 4 * g);
;             const f32x4 x1 = v[ni], x2 = v[ni + hp];
;             v[ni] = x1 * cs - x2 * sn; v[ni + hp] = x2 * cs + x1 * sn;
;         }
; DEVINL void phase2(const Params& P, unsigned char* smem, XPre& X, const bool have_pre) {
;     ...
;                 LOADP(3, ks + 3);                            __builtin_amdgcn_sched_barrier(0);
;                 STEP(0, ks);     __builtin_amdgcn_sched_barrier(0); LOADP(0, ks + 4 < 32 ? ks + 4 : 31); __builtin_amdgcn_sched_barrier(0);
;                 STEP(1, ks + 1); __builtin_amdgcn_sched_barrier(0); LOADP(1, ks + 5 < 32 ? ks + 5 : 31); __builtin_amdgcn_sched_barrier(0);
;                 STEP(2, ks + 2); __builtin_amdgcn_sched_barrier(0); LOADP(2, ks + 6 < 32 ? ks + 6 : 31); __builtin_amdgcn_sched_barrier(0);
;                 STEP(3, ks + 3); __builtin_amdgcn_sched_barrier(0);
;             }
	v_lshl_add_u64 v[60:61], v[196:197], 0, s[0:1]
	s_mov_b32 s7, 0x46c000
	v_add_co_u32_e32 v64, vcc, s7, v60
	s_nop 1
	v_addc_co_u32_e32 v65, vcc, 0, v61, vcc
	global_load_dwordx4 v[60:63], v[64:65], off
	s_nop 0
	global_load_dwordx4 v[64:67], v[64:65], off offset:2048
	v_add_u32_e32 v104, -4, v58
	v_xor_b32_e32 v104, v104, v181
	v_lshl_add_u32 v104, v104, 4, v212
	v_add_u32_e32 v105, 0x10000, v104
	ds_read_b128 v[86:89], v104
	ds_read_b128 v[90:93], v104 offset:32768
	ds_read_b128 v[94:97], v105
	ds_read_b128 v[98:101], v105 offset:32768
	s_waitcnt vmcnt(7) lgkmcnt(7)
	v_mfma_f32_16x16x32_bf16 v[54:57], v[38:41], v[68:71], v[54:57]
	s_waitcnt vmcnt(6)
	v_mfma_f32_16x16x32_bf16 v[50:53], v[42:45], v[68:71], v[50:53]
	s_waitcnt lgkmcnt(6)
	v_mfma_f32_16x16x32_bf16 v[46:49], v[38:41], v[72:75], v[46:49]
	v_mfma_f32_16x16x32_bf16 v[30:33], v[42:45], v[72:75], v[30:33]
	s_waitcnt lgkmcnt(5)
	v_mfma_f32_16x16x32_bf16 v[14:17], v[38:41], v[76:79], v[14:17]
	v_mfma_f32_16x16x32_bf16 v[10:13], v[42:45], v[76:79], v[10:13]
	s_waitcnt lgkmcnt(4)
	v_mfma_f32_16x16x32_bf16 v[6:9], v[38:41], v[80:83], v[6:9]
	v_mfma_f32_16x16x32_bf16 v[2:5], v[42:45], v[80:83], v[2:5]
	v_xor_b32_e32 v104, v58, v181
	v_lshl_add_u32 v104, v104, 4, v212
	v_add_u32_e32 v105, 0x10000, v104
	ds_read_b128 v[68:71], v104
	ds_read_b128 v[72:75], v104 offset:32768
	ds_read_b128 v[76:79], v105
	ds_read_b128 v[80:83], v105 offset:32768
	s_waitcnt vmcnt(5) lgkmcnt(7)
	v_mfma_f32_16x16x32_bf16 v[54:57], v[18:21], v[86:89], v[54:57]
	s_waitcnt vmcnt(4)
	v_mfma_f32_16x16x32_bf16 v[50:53], v[22:25], v[86:89], v[50:53]
	s_waitcnt lgkmcnt(6)
	v_mfma_f32_16x16x32_bf16 v[46:49], v[18:21], v[90:93], v[46:49]
	v_mfma_f32_16x16x32_bf16 v[30:33], v[22:25], v[90:93], v[30:33]
	s_waitcnt lgkmcnt(5)
	v_mfma_f32_16x16x32_bf16 v[14:17], v[18:21], v[94:97], v[14:17]
	v_mfma_f32_16x16x32_bf16 v[10:13], v[22:25], v[94:97], v[10:13]
	s_waitcnt lgkmcnt(4)
	v_mfma_f32_16x16x32_bf16 v[6:9], v[18:21], v[98:101], v[6:9]
	v_mfma_f32_16x16x32_bf16 v[2:5], v[22:25], v[98:101], v[2:5]
	v_add_u32_e32 v104, 4, v58
	v_xor_b32_e32 v104, v104, v181
	v_lshl_add_u32 v104, v104, 4, v212
	v_add_u32_e32 v105, 0x10000, v104
	ds_read_b128 v[86:89], v104
	ds_read_b128 v[90:93], v104 offset:32768
	ds_read_b128 v[94:97], v105
	ds_read_b128 v[98:101], v105 offset:32768
	s_waitcnt vmcnt(3) lgkmcnt(7)
	v_mfma_f32_16x16x32_bf16 v[54:57], v[26:29], v[68:71], v[54:57]
	s_waitcnt vmcnt(2)
	v_mfma_f32_16x16x32_bf16 v[50:53], v[34:37], v[68:71], v[50:53]
	s_waitcnt lgkmcnt(6)
	v_mfma_f32_16x16x32_bf16 v[46:49], v[26:29], v[72:75], v[46:49]
	v_mfma_f32_16x16x32_bf16 v[30:33], v[34:37], v[72:75], v[30:33]
	s_waitcnt lgkmcnt(5)
	v_mfma_f32_16x16x32_bf16 v[14:17], v[26:29], v[76:79], v[14:17]
	v_mfma_f32_16x16x32_bf16 v[10:13], v[34:37], v[76:79], v[10:13]
	s_waitcnt lgkmcnt(4)
	v_mfma_f32_16x16x32_bf16 v[6:9], v[26:29], v[80:83], v[6:9]
	v_mfma_f32_16x16x32_bf16 v[2:5], v[34:37], v[80:83], v[2:5]
	v_add_u32_e32 v58, 16, v58
	v_add_u32_e32 v104, -8, v58
	v_xor_b32_e32 v104, v104, v181
	v_lshl_add_u32 v104, v104, 4, v212
	v_add_u32_e32 v105, 0x10000, v104
	ds_read_b128 v[68:71], v104
	ds_read_b128 v[72:75], v104 offset:32768
	ds_read_b128 v[76:79], v105
	ds_read_b128 v[80:83], v105 offset:32768
	s_waitcnt vmcnt(1) lgkmcnt(7)
	v_mfma_f32_16x16x32_bf16 v[54:57], v[60:63], v[86:89], v[54:57]
	s_waitcnt vmcnt(0)
	v_mfma_f32_16x16x32_bf16 v[50:53], v[64:67], v[86:89], v[50:53]
	s_waitcnt lgkmcnt(6)
	v_mfma_f32_16x16x32_bf16 v[46:49], v[60:63], v[90:93], v[46:49]
	v_mfma_f32_16x16x32_bf16 v[30:33], v[64:67], v[90:93], v[30:33]
	s_waitcnt lgkmcnt(5)
	v_mfma_f32_16x16x32_bf16 v[14:17], v[60:63], v[94:97], v[14:17]
	v_mfma_f32_16x16x32_bf16 v[10:13], v[64:67], v[94:97], v[10:13]
	s_waitcnt lgkmcnt(4)
	v_mfma_f32_16x16x32_bf16 v[6:9], v[60:63], v[98:101], v[6:9]
	v_mfma_f32_16x16x32_bf16 v[2:5], v[64:67], v[98:101], v[2:5]
	s_waitcnt vmcnt(3) lgkmcnt(0)
	v_mov_b32_e32 v20, v180
	s_and_b64 vcc, s[20:21], exec
	s_waitcnt vmcnt(2)
	v_and_or_b32 v24, v20, 15, s62
	v_and_b32_e32 v18, -16, v20
	v_add_u32_e32 v22, s25, v18
	v_add_u32_e32 v23, s81, v18
	v_lshlrev_b32_e32 v178, 7, v24
	s_cbranch_vccz .LBB0_196
	v_add_u32_e32 v18, v23, v178
	s_waitcnt vmcnt(1)
	ds_read_b128 v[26:29], v18
	v_add_u32_e32 v18, v22, v178
	s_waitcnt vmcnt(0)
	ds_read_b128 v[34:37], v18
	s_waitcnt lgkmcnt(1)
	v_pk_mul_f32 v[18:19], v[52:53], v[28:29]
	v_pk_mul_f32 v[38:39], v[50:51], v[26:27]
	s_waitcnt lgkmcnt(0)
	v_pk_fma_f32 v[18:19], v[56:57], v[36:37], v[18:19] neg_lo:[0,0,1] neg_hi:[0,0,1]
	v_pk_fma_f32 v[38:39], v[54:55], v[34:35], v[38:39] neg_lo:[0,0,1] neg_hi:[0,0,1]
	v_pk_mul_f32 v[28:29], v[56:57], v[28:29]
	v_pk_mul_f32 v[26:27], v[54:55], v[26:27]
	v_pk_fma_f32 v[52:53], v[52:53], v[36:37], v[28:29]
	v_pk_fma_f32 v[50:51], v[50:51], v[34:35], v[26:27]
	v_mov_b32_e32 v54, v38
	v_mov_b32_e32 v55, v39
	v_mov_b32_e32 v56, v18
	v_mov_b32_e32 v57, v19
